# copy split retuned for the faster copy loops: N1 30720 -> 32768 items in the in-projection phase
# baseline (speedup 1.0000x reference)
; #define LAS __attribute__((address_space(3)))
; __device__ __forceinline__ int lane_id_v() { int l; asm volatile("v_mbcnt_lo_u32_b32 %0, -1, 0\n\tv_mbcnt_hi_u32_b32 %0, -1, %0" : "=v"(l)); return l; }
; __device__ __forceinline__ XItem xitem(const float* w_gate, const float* w_up, const float* w_down, bf16* BTGU, bf16* BTD, int r) {
;     ...
;     { const int per = (DFF / 128) * (DM / 32); const int e = r / per, r3 = r % per; const int nblk = DM / 32, kb = r3 / nblk, nb = r3 % nblk;
;         it.src = w_down + (size_t)e * DFF * DM + (size_t)(128 * kb) * DM + 32 * nb; it.ldw = DM; it.dst = (unsigned char*)BTD + ((size_t)e * DM + 32 * nb) * DFF + 128 * kb; it.ldd = DFF; it.f8 = 1; return it; }
; __device__ __forceinline__ void convert_range(const float* w_gate, const float* w_up, const float* w_down, bf16* BTGU, bf16* BTD, int x0, int x1, LAS unsigned char* scr, int lane) {
;     if (x0 >= x1) return;
;     f32x4 ta[16], tc[16];
;     XItem A = xitem(w_gate, w_up, w_down, BTGU, BTD, x0), B = A;
;     t64_load(A.src, A.ldw, lane, ta);
; __global__ void __launch_bounds__(512, 2) hymba_fwd(Args args) {
;     ...
;         {   const int lane = lane_id_v();
;             const int nb = FB > 0 ? FB : G, ti = FB > 0 ? bx - GG : bx;
;             if (ti >= 0) { const int q = (CV_N1 + nb * 8 - 1) / (nb * 8), x0 = (ti * 8 + wave) * q, x1 = (x0 + q < CV_N1) ? x0 + q : CV_N1;
;                 convert_range(args.w_gate, args.w_up, args.w_down, BTGU, BTD, x0, x1, lds + wave * 8448, lane); }
.LBB0_140:
	s_sub_i32 s9, s3, s93
	s_cmp_gt_i32 s9, 0
	s_cselect_b64 s[0:1], -1, 0
	s_and_b64 s[20:21], s[0:1], exec
	s_cselect_b32 s8, s93, 0
	s_sub_i32 s8, s2, s8
	s_cmp_lt_i32 s8, 0
	v_readlane_b32 s93, v255, 4
	v_mbcnt_lo_u32_b32 v64, -1, 0
	v_mbcnt_hi_u32_b32 v64, -1, v64
	s_cbranch_scc1 .LBB0_150
	s_and_b64 s[0:1], s[0:1], exec
	s_cselect_b32 s0, s9, s3
	s_lshl_b32 s0, s0, 3
	s_abs_i32 s1, s0
	v_cvt_f32_u32_e32 v0, s1
	s_sub_i32 s20, 0, s1
	s_add_i32 s9, s0, 0x7fff
	s_xor_b32 s0, s9, s0
	v_rcp_iflag_f32_e32 v0, v0
	s_abs_i32 s9, s9
	s_ashr_i32 s0, s0, 31
	v_mul_f32_e32 v0, 0x4f7ffffe, v0
	v_cvt_u32_f32_e32 v0, v0
	s_nop 0
	v_readfirstlane_b32 s21, v0
	s_mul_i32 s20, s20, s21
	s_mul_hi_u32 s20, s21, s20
	s_add_i32 s21, s21, s20
	s_mul_hi_u32 s20, s9, s21
	s_mul_i32 s21, s20, s1
	s_sub_i32 s9, s9, s21
	s_add_i32 s22, s20, 1
	s_sub_i32 s21, s9, s1
	s_cmp_ge_u32 s9, s1
	s_cselect_b32 s20, s22, s20
	s_cselect_b32 s9, s21, s9
	s_add_i32 s21, s20, 1
	s_cmp_ge_u32 s9, s1
	s_cselect_b32 s1, s21, s20
	s_lshl_b32 s8, s8, 3
	s_xor_b32 s1, s1, s0
	s_sub_i32 s0, s1, s0
	s_add_i32 s8, s8, s92
	s_mul_i32 s56, s0, s8
	s_add_i32 s0, s56, s0
	s_min_i32 s52, s0, 0x8000
	s_cmp_ge_i32 s56, s52
	s_cbranch_scc1 .LBB0_150
	s_mul_i32 s0, s92, 0x2100
	s_add_i32 s8, s0, 0
	s_ashr_i32 s0, s56, 31
	s_lshr_b32 s0, s0, 22
	s_add_i32 s1, s56, s0
	s_ashr_i32 s0, s1, 10
	s_and_b32 s1, s1, 0xfffffc00
	s_sub_i32 s1, s56, s1
	s_lshr_b32 s9, s1, 22
	s_and_b32 s9, s9, 0x1ff
	s_add_i32 s9, s1, s9
	s_sext_i32_i16 s20, s9
	s_and_b32 s9, s9, 0xfe00
	s_sub_i32 s9, s1, s9
	s_ashr_i32 s22, s20, 9
	s_sext_i32_i16 s20, s9
	s_bfe_u32 s20, s20, 0x5001a
	s_add_i32 s20, s9, s20
	s_sext_i32_i16 s23, s20
	s_and_b32 s20, s20, 0xffe0
	s_sub_i32 s9, s9, s20
	s_addk_i32 s1, 0x1ff
	s_cmpk_lt_u32 s1, 0x3ff
	s_cselect_b32 s33, s29, s31
	s_cselect_b32 s40, s28, s30
	s_ashr_i32 s1, s0, 31
	s_lshl_b64 s[20:21], s[0:1], 23
	s_sext_i32_i16 s9, s9
	s_add_u32 s54, s40, s20
	s_addc_u32 s21, s33, s21
	s_lshl_b32 s20, s9, 5
	s_lshl_b32 s9, s9, 6
	s_and_b32 s9, s9, 0xffffff00
	s_lshl_b32 s22, s22, 7
	s_add_i32 s9, s9, s22
	s_and_b32 s22, s20, 0x60
	s_or_b32 s22, s9, s22
	s_lshl_b32 s9, s23, 2
	s_and_b32 s40, s9, 0xffffff80
	s_ashr_i32 s41, s40, 31
	s_lshl_b64 s[62:63], s[40:41], 12
	s_add_u32 s9, s54, s62
	s_addc_u32 s23, s21, s63
	s_ashr_i32 s21, s20, 31
	s_lshl_b64 s[20:21], s[20:21], 2
	v_ashrrev_i32_e32 v66, 3, v64
	s_add_u32 s20, s9, s20
	v_ashrrev_i32_e32 v67, 31, v66
	v_lshlrev_b32_e32 v0, 2, v64
	s_addc_u32 s21, s23, s21
	v_and_b32_e32 v128, 28, v0
	v_lshlrev_b64 v[132:133], 12, v[66:67]
	v_mov_b32_e32 v131, 0
	v_lshl_add_u64 v[0:1], s[20:21], 0, v[132:133]
	v_lshlrev_b32_e32 v130, 2, v128
	v_lshl_add_u64 v[0:1], v[0:1], 0, v[130:131]
	s_mov_b32 s9, 0x78000
	v_add_co_u32_e32 v2, vcc, s9, v0
	s_mov_b32 s9, 0x70000
	s_nop 0
	v_addc_co_u32_e32 v3, vcc, 0, v1, vcc
	s_waitcnt vmcnt(0)
; #define LAS __attribute__((address_space(3)))
; #define LDS_WAIT() asm volatile("s_waitcnt lgkmcnt(0)" ::: "memory")
; __device__ __forceinline__ void t64_load(const float* Wsrc, int ldw, int lane, f32x4 (&tv)[16]) {
;     const float* p = Wsrc + (size_t)(lane >> 3) * ldw + 4 * (lane & 7);
; #pragma unroll
;     for (int i = 0; i < 16; ++i) { tv[i] = __builtin_nontemporal_load((const f32x4*)p); p += 8 * ldw; }
; }
; __device__ __forceinline__ void t64_finish(const f32x4 (&tv)[16], unsigned char* dst, int ldd, int f8, LAS unsigned char* scr, int lane) {
;     const int g = lane >> 4, i16 = lane & 15;
; #pragma unroll
;     for (int i = 0; i < 16; ++i) { v2u w; w.x = cvt_pk_bf16(tv[i].x, tv[i].y); w.y = cvt_pk_bf16(tv[i].z, tv[i].w); *(LAS v2u*)(scr + (8 * i + (lane >> 3)) * 64 + 8 * (lane & 7)) = w; }
;     LDS_WAIT(); asm volatile("" ::: "memory");
;     const int q = i16 >> 2, pp = i16 & 3;
;     bf16x8 o[8];
; #pragma unroll
;     for (int jj = 0; jj < 8; ++jj) { const int c = 4 * jj + g, nb = c & 1, kg = c >> 1;
;         LAS unsigned char* ra = scr + (8 * kg + q) * 64 + 32 * nb + 8 * pp;
;         const s16x4 lo = __builtin_bit_cast(s16x4, __builtin_amdgcn_ds_read_tr16_b64_v4i16((LAS s16x4*)ra));
;         const s16x4 hi = __builtin_bit_cast(s16x4, __builtin_amdgcn_ds_read_tr16_b64_v4i16((LAS s16x4*)(ra + 4 * 64)));
;         o[jj] = __builtin_shufflevector(lo, hi, 0, 1, 2, 3, 4, 5, 6, 7); }
;     LDS_WAIT(); asm volatile("" ::: "memory");
; #pragma unroll
;     for (int jj = 0; jj < 8; ++jj) { const int c = 4 * jj + g, nb = c & 1, kg = c >> 1; const int n = 16 * nb + i16;
;         *(LAS bf16x8*)(scr + n * 256 + 16 * (kg ^ (n & 15))) = o[jj]; }
;     LDS_WAIT(); asm volatile("" ::: "memory");
;     const int rr = lane >> 3, cc = lane & 7;
; #pragma unroll
;     for (int it = 0; it < 4; ++it) { const int n = 8 * it + rr;
;         const v4u v0 = *(const LAS v4u*)(scr + n * 256 + 16 * ((2 * cc) ^ (n & 15))), v1 = *(const LAS v4u*)(scr + n * 256 + 16 * ((2 * cc + 1) ^ (n & 15)));
; __device__ __forceinline__ void convert_range(const float* w_gate, const float* w_up, const float* w_down, bf16* BTGU, bf16* BTD, int x0, int x1, LAS unsigned char* scr, int lane) {
;     ...
;     t64_load(A.src, A.ldw, lane, ta);
	v_add_co_u32_e32 v4, vcc, s9, v0
	s_mov_b32 s9, 0x68000
	s_nop 0
	v_addc_co_u32_e32 v5, vcc, 0, v1, vcc
	v_add_co_u32_e32 v6, vcc, s9, v0
	s_mov_b32 s9, 0x60000
	s_nop 0
	v_addc_co_u32_e32 v7, vcc, 0, v1, vcc
	global_load_dwordx4 v[56:59], v[4:5], off nt
	global_load_dwordx4 v[28:31], v[6:7], off nt
	v_add_co_u32_e32 v4, vcc, s9, v0
	s_mov_b32 s9, 0x58000
	s_nop 0
	v_addc_co_u32_e32 v5, vcc, 0, v1, vcc
	v_add_co_u32_e32 v6, vcc, s9, v0
	s_mov_b32 s9, 0x50000
	s_nop 0
	v_addc_co_u32_e32 v7, vcc, 0, v1, vcc
	global_load_dwordx4 v[52:55], v[4:5], off nt
	global_load_dwordx4 v[24:27], v[6:7], off nt
	v_add_co_u32_e32 v4, vcc, s9, v0
	s_mov_b32 s9, 0x48000
	s_nop 0
	v_addc_co_u32_e32 v5, vcc, 0, v1, vcc
	v_add_co_u32_e32 v6, vcc, s9, v0
	s_mov_b32 s9, 0x40000
	s_nop 0
	v_addc_co_u32_e32 v7, vcc, 0, v1, vcc
	global_load_dwordx4 v[48:51], v[4:5], off nt
	global_load_dwordx4 v[20:23], v[6:7], off nt
	v_add_co_u32_e32 v4, vcc, s9, v0
	s_mov_b32 s9, 0x38000
	s_nop 0
	v_addc_co_u32_e32 v5, vcc, 0, v1, vcc
	v_add_co_u32_e32 v6, vcc, s9, v0
	s_mov_b32 s9, 0x30000
	s_nop 0
	v_addc_co_u32_e32 v7, vcc, 0, v1, vcc
	global_load_dwordx4 v[44:47], v[4:5], off nt
	global_load_dwordx4 v[16:19], v[6:7], off nt
	v_add_co_u32_e32 v4, vcc, s9, v0
	s_mov_b32 s9, 0x28000
	s_nop 0
	v_addc_co_u32_e32 v5, vcc, 0, v1, vcc
	v_add_co_u32_e32 v6, vcc, s9, v0
	s_mov_b32 s9, 0x20000
	s_nop 0
	v_addc_co_u32_e32 v7, vcc, 0, v1, vcc
	global_load_dwordx4 v[40:43], v[4:5], off nt
	global_load_dwordx4 v[12:15], v[6:7], off nt
	v_add_co_u32_e32 v4, vcc, s9, v0
	s_mov_b32 s9, 0x18000
	s_nop 0
	v_addc_co_u32_e32 v5, vcc, 0, v1, vcc
	v_add_co_u32_e32 v6, vcc, s9, v0
	s_mov_b32 s9, 0x10000
	s_nop 0
	v_addc_co_u32_e32 v7, vcc, 0, v1, vcc
	global_load_dwordx4 v[36:39], v[4:5], off nt
	global_load_dwordx4 v[8:11], v[6:7], off nt
	v_add_co_u32_e32 v4, vcc, s9, v0
	s_mov_b32 s9, 0x8000
	s_nop 0
	v_addc_co_u32_e32 v5, vcc, 0, v1, vcc
	v_add_co_u32_e32 v6, vcc, s9, v0
	v_lshlrev_b32_e32 v65, 3, v64
	s_nop 0
	v_addc_co_u32_e32 v7, vcc, 0, v1, vcc
	global_load_dwordx4 v[32:35], v[4:5], off nt
	s_nop 0
	global_load_dwordx4 v[4:7], v[6:7], off nt
	s_nop 0
	global_load_dwordx4 v[60:63], v[2:3], off nt
	s_nop 0
	global_load_dwordx4 v[0:3], v[0:1], off nt
	v_and_b32_e32 v68, 0xffffffc0, v65
	v_add_u32_e32 v72, s8, v68
	v_ashrrev_i32_e32 v68, 4, v64
	v_lshlrev_b32_e32 v71, 5, v68
	v_and_b32_e32 v73, 56, v65
	v_bfe_u32 v69, v64, 2, 2
	v_lshlrev_b32_e32 v70, 2, v68
	v_and_b32_e32 v71, 32, v71
	v_and_b32_e32 v65, 24, v65
	s_mov_b32 s9, 0x3fffff8
	v_add3_u32 v129, s8, v71, v65
	v_and_or_b32 v65, v70, s9, v69
	v_lshlrev_b32_e32 v146, 6, v65
	v_lshlrev_b32_e32 v65, 8, v64
	v_and_b32_e32 v65, 0x1f00, v65
	v_add_u32_e32 v81, s8, v65
	v_ashrrev_i32_e32 v65, 5, v64
	v_bitop3_b32 v65, v65, v64, 15 bitop3:0x78
	v_lshlrev_b32_e32 v82, 4, v65
	v_add_u32_e32 v65, 4, v68
	v_lshrrev_b32_e32 v65, 1, v65
	v_bitop3_b32 v65, v65, v64, 15 bitop3:0x78
	v_lshlrev_b32_e32 v83, 4, v65
	v_add_u32_e32 v65, 8, v68
	v_lshrrev_b32_e32 v65, 1, v65
	v_bitop3_b32 v65, v65, v64, 15 bitop3:0x78
	v_lshlrev_b32_e32 v84, 4, v65
	v_add_u32_e32 v65, 12, v68
	v_lshrrev_b32_e32 v65, 1, v65
	v_bitop3_b32 v65, v65, v64, 15 bitop3:0x78
	v_lshlrev_b32_e32 v85, 4, v65
	v_add_u32_e32 v65, 16, v68
	v_lshrrev_b32_e32 v65, 1, v65
	v_bitop3_b32 v65, v65, v64, 15 bitop3:0x78
	v_lshlrev_b32_e32 v86, 4, v65
	v_add_u32_e32 v65, 20, v68
	v_lshrrev_b32_e32 v65, 1, v65
	v_bitop3_b32 v65, v65, v64, 15 bitop3:0x78
	v_lshlrev_b32_e32 v87, 4, v65
	v_add_u32_e32 v65, 24, v68
	v_lshrrev_b32_e32 v65, 1, v65
	v_bitop3_b32 v65, v65, v64, 15 bitop3:0x78
	v_lshlrev_b32_e32 v88, 4, v65
	v_add_u32_e32 v65, 28, v68
	s_ashr_i32 s23, s22, 31
	v_lshrrev_b32_e32 v65, 1, v65
	s_lshl_b64 s[0:1], s[0:1], 22
	s_lshl_b64 s[22:23], s[22:23], 11
	v_bitop3_b32 v65, v65, v64, 15 bitop3:0x78
	v_and_b32_e32 v64, 7, v64
	s_add_u32 s0, s35, s0
	v_lshlrev_b32_e32 v71, 1, v64
	v_lshlrev_b32_e32 v134, 4, v64
	v_and_b32_e32 v64, 15, v66
	s_addc_u32 s1, s53, s1
	v_bitop3_b32 v64, v71, v64, 1 bitop3:0x36
	s_add_u32 s0, s0, s22
	v_lshlrev_b32_e32 v89, 4, v65
	v_bitop3_b32 v65, v66, v71, 15 bitop3:0x6c
	v_lshlrev_b32_e32 v149, 4, v64
	v_add_u32_e32 v64, 8, v66
	v_add_u32_e32 v70, 24, v66
	s_addc_u32 s1, s1, s23
	v_or_b32_e32 v90, 1, v71
	v_lshlrev_b32_e32 v148, 4, v65
	v_bitop3_b32 v65, v64, v71, 15 bitop3:0x6c
	v_bitop3_b32 v71, v70, v71, 15 bitop3:0x6c
	s_add_u32 s0, s0, s40
	v_lshlrev_b32_e32 v92, 4, v65
	v_bitop3_b32 v65, v64, v90, 15 bitop3:0x6c
	v_add_u32_e32 v68, 16, v66
	v_lshlrev_b32_e32 v95, 4, v71
	v_bitop3_b32 v71, v70, v90, 15 bitop3:0x6c
	s_addc_u32 s1, s1, s41
	v_add_u32_e32 v74, 0x400, v146
	v_add_u32_e32 v75, 0x800, v146
	v_add_u32_e32 v76, 0xc00, v146
	v_add_u32_e32 v77, 0x1000, v146
	v_add_u32_e32 v78, 0x1400, v146
	v_add_u32_e32 v79, 0x1800, v146
	v_add_u32_e32 v80, 0x1c00, v146
	v_lshl_add_u32 v91, v64, 8, s8
	v_lshlrev_b32_e32 v93, 4, v65
	v_ashrrev_i32_e32 v65, 31, v64
	v_ashrrev_i32_e32 v69, 31, v68
	v_lshl_add_u32 v94, v70, 8, s8
	v_lshlrev_b32_e32 v90, 4, v71
	v_ashrrev_i32_e32 v71, 31, v70
	v_mov_b32_e32 v135, v131
	v_lshl_add_u32 v147, v66, 8, s8
	v_lshl_add_u32 v150, v68, 8, s8
	v_lshlrev_b64 v[136:137], 11, v[66:67]
	v_lshlrev_b64 v[138:139], 11, v[64:65]
	v_lshlrev_b64 v[140:141], 11, v[68:69]
	v_lshlrev_b64 v[142:143], 11, v[70:71]
	v_add_u32_e32 v151, v72, v73
	v_add_u32_e32 v152, v129, v74
	v_add_u32_e32 v153, v129, v75
	v_add_u32_e32 v154, v129, v76
	v_add_u32_e32 v155, v129, v77
	v_add_u32_e32 v156, v129, v78
	v_add_u32_e32 v157, v129, v79
	v_add_u32_e32 v158, v129, v80
	v_add_u32_e32 v159, v81, v82
	v_add_u32_e32 v160, v81, v83
	v_add_u32_e32 v161, v81, v84
	v_add_u32_e32 v162, v81, v85
	v_add_u32_e32 v163, v81, v86
	v_add_u32_e32 v164, v81, v87
	v_add_u32_e32 v165, v81, v88
	v_add_u32_e32 v166, v81, v89
	v_add_u32_e32 v167, v91, v92
	v_add_u32_e32 v168, v91, v93
	v_add_u32_e32 v169, v94, v95
	v_add_u32_e32 v170, v94, v90
	s_mov_b64 s[8:9], s[0:1]
	s_branch .LBB0_145

; #define LAS __attribute__((address_space(3)))
; #define TID() (wave * 64 + lane_id_v())
; __global__ void __launch_bounds__(512, 2) hymba_fwd(Args args) {
;     ...
;         LAS float* btab = (LAS float*)(lds + 8 * 12288);
;         const int tid = TID(), lane = tid & 63;
;         {
;             LAS float* rb = (LAS float*)(lds + 8 * 12288 + NH * 396 * 4);
;             LAS float* mhs = rb + 512;
;             LAS unsigned char* kbl = (LAS unsigned char*)(mhs + 16);
;             static_assert(8 * 12288 + NH * 396 * 4 + 2048 + 64 + 400 <= 131072, "P2 table scratch below the MoE tables");
;             rb[tid] = args.rel_bias[tid];
;             if (tid < 396) kbl[tid] = kBucket[tid / 132][tid % 132];
;             float gq = fabsf(args.q_norm_g[lane]), gk = fabsf(args.k_norm_g[lane]);
; #pragma unroll
;             for (int o = 1; o < 64; o <<= 1) { gq = fmaxf(gq, __shfl_xor(gq, o)); gk = fmaxf(gk, __shfl_xor(gk, o)); }
;             __syncthreads();
;             if (tid < NH) { float mb = 0.f; for (int b = 0; b < 32; ++b) mb = fmaxf(mb, fabsf(rb[b * NH + tid])); mhs[tid] = 1.02f * C2 * 64.f * gq * gk + mb * LOG2E; }
;             __syncthreads();
;             for (int idx = tid; idx < NH * 3 * 132; idx += 512) { const int h = idx / 396, r2 = idx % 396;
;                 btab[idx] = rb[(int)kbl[r2] * NH + h] * LOG2E - mhs[h]; }
;         }
;         __syncthreads();
;         LAS unsigned char* vbuf = lds + wave * 12288;
;     ...
;             constexpr int CV_LO = CV_N1, CV_HI = CV_GU + CV_D - CV_N5, CV_EXP = CV_HI - CV_LO;
;             const int nA = (512 - bx + G - 1) / G;
;             const int per_wave = (CV_EXP + NGW - 1) / NGW;
;             const int c_lo = CV_LO + gw * per_wave, c_hi = (c_lo + per_wave < CV_HI) ? c_lo + per_wave : CV_HI;
;             const int nsteps = nA > 0 ? nA : 1, per_batch = (per_wave + nsteps - 1) / nsteps;
;             int ia = 0, ic = c_lo;
.LBB0_212:
	s_or_b64 exec, exec, s[0:1]
	s_abs_i32 s0, s3
	v_cvt_f32_u32_e32 v1, s0
	s_mul_i32 s1, s92, 0x3000
	s_add_i32 s68, s1, 0
	s_sub_i32 s1, s3, s2
	v_rcp_iflag_f32_e32 v1, v1
	s_add_i32 s6, s1, 0x1ff
	s_sub_i32 s1, 0xfffffe01, s1
	s_xor_b32 s7, s6, s3
	v_mul_f32_e32 v1, 0x4f7ffffe, v1
	v_cvt_u32_f32_e32 v1, v1
	s_max_i32 s1, s6, s1
	s_sub_i32 s6, 0, s0
	s_ashr_i32 s7, s7, 31
	v_readfirstlane_b32 s20, v1
	s_mul_i32 s6, s6, s20
	s_mul_hi_u32 s6, s20, s6
	s_add_i32 s20, s20, s6
	s_mul_hi_u32 s6, s1, s20
	s_mul_i32 s20, s6, s0
	s_sub_i32 s1, s1, s20
	s_add_i32 s20, s6, 1
	s_sub_i32 s21, s1, s0
	s_cmp_ge_u32 s1, s0
	s_cselect_b32 s6, s20, s6
	s_cselect_b32 s1, s21, s1
	s_add_i32 s20, s6, 1
	s_cmp_ge_u32 s1, s0
	s_cselect_b32 s0, s20, s6
	s_abs_i32 s6, s90
	v_cvt_f32_u32_e32 v1, s6
	s_sub_i32 s20, 0, s6
	s_xor_b32 s0, s0, s7
	s_sub_i32 s69, s0, s7
	v_rcp_iflag_f32_e32 v1, v1
	s_add_i32 s0, s90, 0x2fff
	s_xor_b32 s7, s0, s90
	s_abs_i32 s0, s0
	v_mul_f32_e32 v1, 0x4f7ffffe, v1
	v_cvt_u32_f32_e32 v1, v1
	s_ashr_i32 s7, s7, 31
	v_lshlrev_b32_e32 v4, 1, v159
	v_lshrrev_b32_e32 v3, 2, v159
	v_readfirstlane_b32 s21, v1
	s_mul_i32 s20, s20, s21
	s_mul_hi_u32 s20, s21, s20
	s_add_i32 s21, s21, s20
	s_mul_hi_u32 s20, s0, s21
	s_mul_i32 s21, s20, s6
	s_sub_i32 s0, s0, s21
	s_add_i32 s21, s20, 1
	s_sub_i32 s22, s0, s6
	s_cmp_ge_u32 s0, s6
	s_cselect_b32 s20, s21, s20
	s_cselect_b32 s0, s22, s0
	s_add_i32 s21, s20, 1
	s_cmp_ge_u32 s0, s6
	s_cselect_b32 s0, s21, s20
	s_max_i32 s6, s69, 1
	v_cvt_f32_u32_e32 v1, s6
	s_xor_b32 s0, s0, s7
	s_sub_i32 s0, s0, s7
	s_mul_i32 s7, s0, s34
	v_rcp_iflag_f32_e32 v1, v1
	v_and_b32_e32 v4, 32, v4
	s_add_i32 s67, s7, 0x8000
	s_sub_i32 s20, 0, s6
	v_mul_f32_e32 v1, 0x4f7ffffe, v1
	v_cvt_u32_f32_e32 v1, v1
	s_add_i32 s7, s67, s0
	s_add_i32 s0, s6, s0
	s_add_i32 s0, s0, -1
	v_readfirstlane_b32 s21, v1
	v_lshlrev_b32_e32 v1, 3, v159
	v_and_b32_e32 v2, 0x1c0, v1
	v_add_u32_e32 v163, s68, v2
	v_and_b32_e32 v165, 56, v1
	v_bfe_u32 v2, v0, 2, 2
	v_and_b32_e32 v1, 24, v1
	v_add3_u32 v167, s68, v4, v1
	v_and_or_b32 v1, v3, 8, v2
	s_mul_i32 s20, s20, s21
	v_lshlrev_b32_e32 v169, 6, v1
	v_lshlrev_b32_e32 v1, 8, v159
	s_mul_hi_u32 s20, s21, s20
	v_and_b32_e32 v1, 0x1f00, v1
	v_lshrrev_b32_e32 v2, 5, v159
	s_min_i32 s66, s7, 0xb000
	s_ashr_i32 s7, s0, 31
	s_abs_i32 s0, s0
	s_add_i32 s21, s21, s20
	v_add_u32_e32 v204, s68, v1
	v_and_b32_e32 v1, 15, v0
	v_bitop3_b32 v3, v2, v0, 15 bitop3:0x78
	s_mul_hi_u32 s20, s0, s21
	v_lshlrev_b32_e32 v205, 4, v3
	v_bitop3_b32 v3, v2, v1, 2 bitop3:0x36
	s_mul_i32 s21, s20, s6
	v_lshlrev_b32_e32 v206, 4, v3
	v_bitop3_b32 v3, v2, v1, 4 bitop3:0x36
	s_sub_i32 s0, s0, s21
	v_lshlrev_b32_e32 v207, 4, v3
	v_bitop3_b32 v3, v2, v1, 6 bitop3:0x36
	s_add_i32 s21, s20, 1
	s_sub_i32 s22, s0, s6
	v_lshlrev_b32_e32 v208, 4, v3
	v_bitop3_b32 v3, v2, v1, 8 bitop3:0x36
	s_cmp_ge_u32 s0, s6
	v_lshlrev_b32_e32 v209, 4, v3
	v_bitop3_b32 v3, v2, v1, 10 bitop3:0x36
	s_cselect_b32 s20, s21, s20
	v_lshlrev_b32_e32 v210, 4, v3
	v_bitop3_b32 v3, v2, v1, 12 bitop3:0x36
	v_bitop3_b32 v1, v2, v1, 14 bitop3:0x36
	v_and_b32_e32 v0, 7, v0
	s_cselect_b32 s0, s22, s0
	s_add_i32 s21, s20, 1
	v_lshrrev_b32_e32 v158, 3, v159
	v_lshlrev_b32_e32 v212, 4, v1
	v_lshlrev_b32_e32 v1, 1, v0
	s_cmp_ge_u32 s0, s6
	v_lshlrev_b32_e32 v160, 4, v0
	v_xor_b32_e32 v0, v158, v1
	s_cselect_b32 s0, s21, s20
	v_lshlrev_b32_e32 v214, 4, v0
	v_bitop3_b32 v0, v1, v158, 1 bitop3:0x36
	s_xor_b32 s0, s0, s7
	v_or_b32_e32 v2, 1, v1
	v_lshlrev_b32_e32 v215, 4, v0
	v_bitop3_b32 v0, v158, v1, 8 bitop3:0x36
	s_sub_i32 s72, s0, s7
	s_lshl_b32 s73, s6, 1
	v_lshlrev_b32_e32 v217, 4, v0
	v_bitop3_b32 v0, v158, v2, 8 bitop3:0x36
	v_or_b32_e32 v166, 24, v158
	s_cmpk_gt_u32 s74, 0xff
	v_lshlrev_b32_e32 v218, 4, v0
	v_bitop3_b32 v0, v166, v1, 15 bitop3:0x6c
	v_mov_b32_e32 v171, 0
	v_or_b32_e32 v162, 8, v158
	v_or_b32_e32 v164, 16, v158
	v_lshlrev_b32_e32 v221, 4, v0
	v_bitop3_b32 v0, v166, v2, 15 bitop3:0x6c
	s_cselect_b64 s[6:7], -1, 0
	s_mov_b32 s20, 0x3f803f80
	s_mov_b32 s1, 0
	s_mov_b32 s96, s74
	v_and_b32_e32 v168, 28, v157
	v_lshlrev_b32_e32 v211, 4, v3
	v_mov_b32_e32 v161, v171
	v_lshl_add_u32 v213, v158, 8, s68
	v_lshl_add_u32 v216, v162, 8, s68
	v_lshl_add_u32 v219, v164, 8, s68
	v_lshl_add_u32 v220, v166, 8, s68
	v_lshlrev_b32_e32 v222, 4, v0
	v_cndmask_b32_e64 v223, 0, 1, s[6:7]
	s_movk_i32 s74, 0x60
	s_add_i32 s75, 0, 0x180b4
	s_mov_b32 s76, 0x5fc0000
	s_mov_b32 s77, 0x6fc0000
	s_mov_b32 s78, 0x5fd0000
	s_mov_b32 s79, 0x6fd0000
	s_mov_b32 s80, 0x5fe0000
	s_mov_b32 s81, 0x6fe0000
	s_mov_b32 s40, 0x3f803f80
	s_mov_b32 s41, s20
	s_mov_b32 s42, s20
	s_mov_b32 s43, s20
	v_mov_b32_e32 v0, 0x3f803f80
	s_mov_b32 s82, 0
	s_mov_b32 s83, 0
	s_waitcnt lgkmcnt(0)
	s_barrier
	s_branch .LBB0_214
